# v63 + finer tail of the attention work queue: stick-breaking entries keep half of their weight-copy chunk, the other halves become 16 extra copy-only entries per XCD (80 entries instead of 64)
# speedup vs baseline: 1.0054x; 1.0054x over previous
.LBB6_896:
	s_or_b64 exec, exec, s[2:3]
	v_readlane_b32 s0, v254, 30
	s_waitcnt lgkmcnt(0)
	s_barrier
	v_mov_b32_e32 v2, s0
	ds_read_b32 v2, v2
	s_mov_b64 s[2:3], -1
	s_waitcnt lgkmcnt(0)
	s_barrier
	v_readfirstlane_b32 s0, v2
	s_cmp_gt_i32 s0, 0x4f
	s_cbranch_scc1 .LBB6_891
	s_cmp_gt_i32 s0, 47
	s_cbranch_scc0 .LBB6_899
	s_sub_i32 s1, s0, 48
	s_lshr_b32 s92, s1, 1
	s_mov_b64 s[2:3], 0

.LBB6_901:
	s_lshl_b32 s84, s0, 3
	s_or_b32 s1, s84, s59
	s_lshl_b32 s2, s1, 1
	s_add_i32 s3, s1, 0x180
	s_cmp_lt_u32 s1, 0x180
	s_cselect_b32 s2, s2, s3
	s_mul_i32 s2, s63, s2
	s_lshr_b32 s2, s2, 10
	s_and_b32 s90, s2, 0xffffffe0
	s_add_i32 s1, s1, 1
	s_lshl_b32 s2, s1, 1
	s_add_i32 s3, s1, 0x180
	s_cmp_lt_u32 s1, 0x180
	s_cselect_b32 s2, s2, s3
	s_mul_i32 s2, s63, s2
	s_lshr_b32 s2, s2, 10
	s_and_b32 s91, s2, 0xffffffe0
	s_bitcmp0_b32 s0, 0
	s_cselect_b64 s[22:23], -1, 0
	s_and_b64 vcc, exec, s[22:23]
	s_cbranch_vccnz .LBB6_1210
	v_readfirstlane_b32 s98, v0
	s_nop 0
	s_bitcmp1_b32 s98, 8
	s_cbranch_scc0 .Ldephase_a
	s_sleep 80

.LBB6_1210:
	s_cmp_ge_u32 s84, 0x200
	s_cbranch_scc1 .LBB6_1306
	s_and_b32 s0, s84, 8
	s_or_b32 s0, s0, s59
	s_sub_i32 s37, 7, s92
	s_lshr_b32 s36, s0, 2
	s_mov_b64 s[6:7], -1
	s_mov_b64 s[2:3], 0
	s_cmp_lt_i32 s93, 1
	s_mov_b64 s[4:5], 0
	s_cbranch_scc1 .LBB6_1224
	s_cmp_gt_i32 s93, 1
	s_cbranch_scc0 .LBB6_1252
	s_cmp_eq_u32 s93, 2
	s_mov_b64 s[4:5], -1
	s_cbranch_scc0 .LBB6_1251
	s_lshl_b32 s1, s37, 8
	s_lshl_b32 s6, s36, 11
	v_readlane_b32 s4, v254, 13
	s_add_i32 s0, s1, 0x100
	s_add_i32 s26, s1, s6
	v_readlane_b32 s5, v254, 14
	s_lshr_b32 s0, s0, 6
	s_mul_i32 s7, s26, 0x600
	s_mul_hi_u32 s6, s26, 0x600
	s_add_u32 s7, s4, s7
	s_addc_u32 s6, s5, s6
	s_add_u32 s7, s7, s71
	s_addc_u32 s6, s6, 0
	s_add_u32 s12, s7, 0x7200000
	s_addc_u32 s13, s6, 0
	s_mul_i32 s6, s36, 0x300000
	s_add_u32 s6, s4, s6
	s_addc_u32 s7, s5, 0
	s_add_u32 s6, s6, s71
	s_addc_u32 s7, s7, 0
	s_add_u32 s6, s6, 0x7e00000
	s_addc_u32 s7, s7, 0
	s_add_u32 s24, s4, s75
	s_addc_u32 s25, s5, 0
	s_lshl_b32 s27, s36, 12
	s_add_u32 s24, s24, s27
	v_mov_b32_e32 v183, v0
	s_addc_u32 s25, s25, 0
	s_waitcnt vmcnt(0)
	v_mov_b32_e32 v34, v0
	s_add_u32 s24, s24, 0xf300000
	s_addc_u32 s25, s25, 0
	v_readfirstlane_b32 s27, v34
	s_ashr_i32 s27, s27, 1
	s_movk_i32 s28, 0xffe0
	v_mov_b32_e32 v2, s27
	v_bfi_b32 v2, s28, v2, v34
	v_mov_b64_e32 v[4:5], s[12:13]
	v_bfe_u32 v35, v34, 5, 1
	v_mad_i64_i32 v[4:5], s[12:13], v2, s70, v[4:5]
	v_lshlrev_b32_e32 v2, 4, v35
	s_mov_b32 s12, 0x2aaaaaab
	v_lshl_add_u64 v[24:25], v[4:5], 0, v[2:3]
	v_mul_hi_i32 v4, v34, s12
	v_lshrrev_b32_e32 v5, 31, v4
	v_ashrrev_i32_e32 v4, 2, v4
	v_add_u32_e32 v189, v4, v5
	v_mul_lo_u32 v4, v189, 24
	v_sub_u32_e32 v36, v34, v4
	v_add_u32_e32 v4, 0x200, v34
	v_mul_hi_i32 v5, v4, s12
	v_lshrrev_b32_e32 v6, 31, v5
	v_ashrrev_i32_e32 v5, 2, v5
	v_add_u32_e32 v190, v5, v6
	v_mul_lo_u32 v5, v190, 24
	v_sub_u32_e32 v37, v4, v5
	v_add_u32_e32 v4, 0x400, v34
	v_mul_hi_i32 v5, v4, s12
	v_lshrrev_b32_e32 v6, 31, v5
	v_ashrrev_i32_e32 v5, 2, v5
	v_add_u32_e32 v192, v5, v6
	v_mul_lo_u32 v5, v192, 24
	v_sub_u32_e32 v38, v4, v5
	v_lshlrev_b32_e32 v14, 3, v38
	v_ashrrev_i32_e32 v15, 31, v14
	v_lshlrev_b32_e32 v6, 3, v36
	v_lshlrev_b32_e32 v8, 3, v37
	v_lshlrev_b64 v[32:33], 1, v[14:15]
	v_lshlrev_b32_e32 v14, 4, v34
	v_ashrrev_i32_e32 v39, 3, v34
	v_mov_b64_e32 v[26:27], s[6:7]
	v_ashrrev_i32_e32 v7, 31, v6
	v_ashrrev_i32_e32 v9, 31, v8
	v_and_b32_e32 v168, 0x70, v14
	v_mov_b32_e32 v169, v3
	v_mad_i64_i32 v[4:5], s[12:13], v189, s70, v[26:27]
	v_lshlrev_b64 v[28:29], 1, v[6:7]
	v_mad_i64_i32 v[6:7], s[12:13], v190, s70, v[26:27]
	v_lshlrev_b64 v[30:31], 1, v[8:9]
	v_mad_i64_i32 v[12:13], s[12:13], v192, s70, v[26:27]
	v_lshl_add_u64 v[170:171], s[24:25], 0, v[168:169]
	v_add_u32_e32 v40, 64, v39
	v_lshl_add_u64 v[4:5], v[4:5], 0, v[28:29]
	v_lshl_add_u64 v[8:9], v[6:7], 0, v[30:31]
	v_lshl_add_u64 v[12:13], v[12:13], 0, v[32:33]
	v_mad_i64_i32 v[16:17], s[12:13], v39, s55, v[170:171]
	v_mad_i64_i32 v[20:21], s[12:13], v40, s55, v[170:171]
	global_load_dwordx4 v[4:7], v[4:5], off
	s_nop 0
	global_load_dwordx4 v[8:11], v[8:9], off
	s_nop 0
	global_load_dwordx4 v[12:15], v[12:13], off
	s_nop 0
	global_load_dwordx4 v[16:19], v[16:17], off
	s_nop 0
	global_load_dwordx4 v[20:23], v[20:21], off
	s_nop 0
	global_load_dwordx4 v[144:147], v[24:25], off
	global_load_dwordx4 v[140:143], v[24:25], off offset:32
	global_load_dwordx4 v[136:139], v[24:25], off offset:64
	global_load_dwordx4 v[132:135], v[24:25], off offset:96
	global_load_dwordx4 v[128:131], v[24:25], off offset:128
	global_load_dwordx4 v[124:127], v[24:25], off offset:160
	global_load_dwordx4 v[120:123], v[24:25], off offset:192
	global_load_dwordx4 v[116:119], v[24:25], off offset:224
	global_load_dwordx4 v[112:115], v[24:25], off offset:256
	global_load_dwordx4 v[108:111], v[24:25], off offset:288
	global_load_dwordx4 v[104:107], v[24:25], off offset:320
	global_load_dwordx4 v[100:103], v[24:25], off offset:352
	v_add_u32_e32 v24, 64, v189
	v_mad_i64_i32 v[24:25], s[12:13], v24, s70, v[26:27]
	v_lshl_add_u64 v[24:25], v[24:25], 0, v[28:29]
	global_load_dwordx4 v[148:151], v[24:25], off
	v_add_u32_e32 v24, 64, v190
	v_mad_i64_i32 v[24:25], s[12:13], v24, s70, v[26:27]
	v_add_u32_e32 v41, 64, v192
	v_lshl_add_u64 v[24:25], v[24:25], 0, v[30:31]
	v_mad_i64_i32 v[26:27], s[12:13], v41, s70, v[26:27]
	v_lshl_add_u64 v[26:27], v[26:27], 0, v[32:33]
	global_load_dwordx4 v[152:155], v[24:25], off
	global_load_dwordx4 v[156:159], v[26:27], off
	v_mov_b64_e32 v[24:25], s[24:25]
	v_mad_i64_i32 v[26:27], s[12:13], v39, s55, v[24:25]
	v_lshl_add_u64 v[26:27], v[26:27], 0, v[168:169]
	v_mad_i64_i32 v[24:25], s[12:13], v40, s55, v[24:25]
	v_lshl_add_u64 v[24:25], v[24:25], 0, v[168:169]
	global_load_dwordx4 v[160:163], v[26:27], off offset:128
	global_load_dwordx4 v[164:167], v[24:25], off offset:128
	s_and_b32 s25, s27, 0xffffffe0
	s_add_i32 s12, s25, s1
	v_lshlrev_b32_e32 v24, 1, v34
	v_lshrrev_b32_e32 v25, 1, v34
	s_movk_i32 s1, 0x190
	v_and_b32_e32 v24, 8, v24
	v_and_b32_e32 v25, 4, v25
	v_and_b32_e32 v26, 19, v34
	v_mul_lo_u32 v194, v189, s1
	v_lshlrev_b32_e32 v195, 4, v36
	v_or3_b32 v24, v24, v26, v25
	v_add3_u32 v25, 0, v194, v195
	v_mul_lo_u32 v196, v190, s1
	v_lshlrev_b32_e32 v197, 4, v37
	v_mul_lo_u32 v198, v192, s1
	v_lshlrev_b32_e32 v199, 4, v38
	v_mul_lo_u32 v201, v39, s41
	v_and_b32_e32 v191, 31, v34
	v_mul_i32_i24_e32 v193, -8, v35
	s_lshl_b32 s1, s92, 8
	v_mad_i64_i32 v[172:173], s[28:29], v39, s55, 0
	v_mad_i64_i32 v[174:175], s[28:29], v40, s55, 0
	v_mul_u32_u24_e32 v200, 0x190, v24
	v_lshl_add_u64 v[176:177], s[6:7], 0, v[28:29]
	v_lshl_add_u64 v[178:179], s[6:7], 0, v[30:31]
	v_lshl_add_u64 v[184:185], s[6:7], 0, v[32:33]
	s_mov_b32 s24, 1
	s_or_b32 s13, s12, 31
	v_mul_u32_u24_e32 v169, 0x90, v191
	v_mov_b32_e32 v187, 0
	v_mov_b32_e32 v188, 0xf149f2ca
	s_movk_i32 s84, 0x80
	s_waitcnt vmcnt(21)
	ds_write_b128 v25, v[4:7]
	v_add3_u32 v4, 0, v196, v197
	s_waitcnt vmcnt(20)
	ds_write_b128 v4, v[8:11]
	v_add3_u32 v4, 0, v198, v199
	s_waitcnt vmcnt(19)
	ds_write_b128 v4, v[12:15]
	v_add3_u32 v4, 0, v168, v201
	s_waitcnt vmcnt(18)
	ds_write_b128 v4, v[16:19] offset:25600
	s_waitcnt vmcnt(17)
	ds_write_b128 v4, v[20:23] offset:34816
	v_add3_u32 v4, v193, s25, v191
	v_subrev_u32_e32 v4, s1, v4
	v_mov_b32_e32 v18, v3
	v_mov_b32_e32 v19, v3
	v_add_u32_e32 v202, 0x6e9, v4
	v_mov_b32_e32 v4, v3
	v_mov_b32_e32 v5, v3
	v_mov_b32_e32 v6, v3
	v_mov_b32_e32 v7, v3
	v_mov_b32_e32 v8, v3
	v_mov_b32_e32 v9, v3
	v_mov_b32_e32 v10, v3
	v_mov_b32_e32 v11, v3
	v_mov_b32_e32 v12, v3
	v_mov_b32_e32 v13, v3
	v_mov_b32_e32 v14, v3
	v_mov_b32_e32 v15, v3
	v_mov_b32_e32 v16, v3
	v_mov_b32_e32 v17, v3
	v_mov_b64_e32 v[34:35], v[18:19]
	v_mov_b64_e32 v[50:51], v[18:19]
	v_mov_b64_e32 v[66:67], v[18:19]
	v_mov_b64_e32 v[32:33], v[16:17]
	v_mov_b64_e32 v[30:31], v[14:15]
	v_mov_b64_e32 v[28:29], v[12:13]
	v_mov_b64_e32 v[26:27], v[10:11]
	v_mov_b64_e32 v[24:25], v[8:9]
	v_mov_b64_e32 v[22:23], v[6:7]
	v_mov_b64_e32 v[20:21], v[4:5]
	v_mov_b64_e32 v[48:49], v[16:17]
	v_mov_b64_e32 v[46:47], v[14:15]
	v_mov_b64_e32 v[44:45], v[12:13]
	v_mov_b64_e32 v[42:43], v[10:11]
	v_mov_b64_e32 v[40:41], v[8:9]
	v_mov_b64_e32 v[38:39], v[6:7]
	v_mov_b64_e32 v[36:37], v[4:5]
	v_mov_b64_e32 v[64:65], v[16:17]
	v_mov_b64_e32 v[62:63], v[14:15]
	v_mov_b64_e32 v[60:61], v[12:13]
	v_mov_b64_e32 v[58:59], v[10:11]
	v_mov_b64_e32 v[56:57], v[8:9]
	v_mov_b64_e32 v[54:55], v[6:7]
	v_mov_b64_e32 v[52:53], v[4:5]
	s_waitcnt lgkmcnt(0)
	s_barrier
